# attention K/V sharing with 3 barriers per unit (V' in flight across K loop + softmax) + dead DMA address arithmetic removed
# baseline (speedup 1.0000x reference)
.LBB0_451:
	s_nop 0
	ds_read_b128 v[50:53], v221 offset:45056
	ds_read_b128 v[66:69], v222 offset:45056
	s_waitcnt lgkmcnt(0)
	v_mfma_f32_32x32x16_bf16 v[50:65], v[50:53], v[158:161], 0
	v_mfma_f32_32x32x16_bf16 v[50:65], v[66:69], v[154:157], v[50:65]
	ds_read_b128 v[66:69], v223 offset:45056
	s_waitcnt lgkmcnt(0)
	v_mfma_f32_32x32x16_bf16 v[50:65], v[66:69], v[150:153], v[50:65]
	ds_read_b128 v[66:69], v224 offset:45056
	s_waitcnt lgkmcnt(0)
	s_waitcnt lgkmcnt(0)
	v_mfma_f32_32x32x16_bf16 v[50:65], v[66:69], v[146:149], v[50:65]
	ds_read_b128 v[66:69], v221 offset:49152
	ds_read_b128 v[82:85], v222 offset:49152
	s_waitcnt lgkmcnt(0)
	v_mfma_f32_32x32x16_bf16 v[66:81], v[66:69], v[158:161], 0
	v_mfma_f32_32x32x16_bf16 v[66:81], v[82:85], v[154:157], v[66:81]
	ds_read_b128 v[82:85], v223 offset:49152
	s_waitcnt lgkmcnt(0)
	v_mfma_f32_32x32x16_bf16 v[66:81], v[82:85], v[150:153], v[66:81]
	ds_read_b128 v[82:85], v224 offset:49152
	s_waitcnt lgkmcnt(0)
	s_waitcnt lgkmcnt(0)
	v_mfma_f32_32x32x16_bf16 v[66:81], v[82:85], v[146:149], v[66:81]
	s_barrier
	s_add_i32 s38, s53, 1
	s_cmp_lt_i32 s38, s0
	s_cselect_b64 s[96:97], -1, 0
	s_cmp_ge_i32 s38, s0
	s_mov_b32 s39, s86
	s_mov_b32 s40, s88
	s_mov_b32 s47, s81
	s_mov_b32 s41, s33
	s_mov_b32 s80, s42
	s_mov_b32 s48, s82
	v_mov_b32_e32 v183, v180
	v_mov_b32_e32 v190, v178
	v_mov_b32_e32 v187, v182
	s_cbranch_scc1 .LBB0_466
	v_readlane_b32 s40, v254, 8
	v_readlane_b32 s41, v254, 9
	s_mov_b64 s[4:5], -1
	s_and_b64 vcc, exec, s[40:41]
	s_cbranch_vccz .LBB0_454
	s_mul_i32 s4, s38, s74
	v_readlane_b32 s40, v254, 19
	s_add_i32 s39, s4, s40
	s_mov_b64 s[4:5], 0

.Latt_b3m:
	s_waitcnt vmcnt(12)
	s_barrier
	ds_read_b64_tr_b16 v[10:11], v195
	ds_read_b64_tr_b16 v[12:13], v195 offset:1024
	ds_read_b64_tr_b16 v[6:7], v196
	ds_read_b64_tr_b16 v[8:9], v196 offset:1024
	s_waitcnt lgkmcnt(0)
	s_nop 0
	v_add_f32_e32 v34, v48, v14
	v_mfma_f32_32x32x16_bf16 v[18:33], v[10:13], v[2:5], 0
	v_sub_f32_e32 v10, v94, v66
	v_exp_f32_e32 v63, v10
	v_sub_f32_e32 v10, v95, v66
	v_exp_f32_e32 v65, v10
	v_sub_f32_e32 v10, v96, v66
	v_exp_f32_e32 v64, v10
	v_sub_f32_e32 v35, v70, v66
	v_mfma_f32_32x32x16_bf16 v[2:17], v[6:9], v[2:5], 0
	v_exp_f32_e32 v70, v35
	v_add_f32_e32 v34, v63, v34
	v_cvt_pk_bf16_f32 v82, v119, v120
	v_cvt_pk_bf16_f32 v83, v121, v122
	v_cvt_pk_bf16_f32 v84, v123, v124
	v_cvt_pk_bf16_f32 v85, v125, v126
	ds_read_b64_tr_b16 v[90:91], v197
	ds_read_b64_tr_b16 v[92:93], v197 offset:1024
	ds_read_b64_tr_b16 v[86:87], v198
	ds_read_b64_tr_b16 v[88:89], v198 offset:1024
	s_waitcnt lgkmcnt(0)
	v_add_f32_e32 v34, v65, v34
	v_mfma_f32_32x32x16_bf16 v[18:33], v[90:93], v[82:85], v[18:33]
	v_add_f32_e32 v34, v64, v34
	v_add_f32_e32 v59, v70, v34
	ds_bpermute_b32 v60, v118, v59
	v_mfma_f32_32x32x16_bf16 v[2:17], v[86:89], v[82:85], v[2:17]
	s_and_b64 vcc, exec, s[72:73]
	s_mov_b64 s[4:5], -1
	s_cbranch_vccnz .LBB0_473
	s_lshl_b32 s90, s37, 1
	s_nop 0
	s_add_i32 m0, s75, 0x800
	s_nop 0
	s_mov_b64 s[4:5], 0
